# grid barriers: all waiters poll the top-level arrival counter; the last arriver's generation-word atomic is removed
# speedup vs baseline: 1.0038x; 1.0038x over previous
.LBB0_123:
	s_or_b64 exec, exec, s[8:9]
	v_cvt_f32_u32_e32 v5, v3
	s_waitcnt vmcnt(0)
	v_readfirstlane_b32 s6, v4
	v_sub_u32_e32 v4, 0, v3
	v_rcp_iflag_f32_e32 v5, v5
	v_add_u32_e32 v6, s6, v2
	v_mul_f32_e32 v5, 0x4f7ffffe, v5
	v_cvt_u32_f32_e32 v5, v5
	v_mul_lo_u32 v2, v4, v5
	v_mul_hi_u32 v2, v5, v2
	v_add_u32_e32 v2, v5, v2
	v_mul_hi_u32 v2, v6, v2
	v_mul_lo_u32 v4, v2, v3
	v_sub_u32_e32 v4, v6, v4
	v_add_u32_e32 v5, 1, v2
	v_cmp_ge_u32_e32 vcc, v4, v3
	s_nop 1
	v_cndmask_b32_e32 v2, v2, v5, vcc
	v_sub_u32_e32 v5, v4, v3
	v_cndmask_b32_e32 v4, v4, v5, vcc
	v_add_u32_e32 v5, 1, v2
	v_cmp_ge_u32_e32 vcc, v4, v3
	v_add_u32_e32 v4, 1, v6
	s_nop 0
	v_cndmask_b32_e32 v2, v2, v5, vcc
	v_mul_lo_u32 v5, v3, v2
	v_add_u32_e32 v3, v5, v3
	v_cmp_ne_u32_e32 vcc, v4, v3
	s_and_saveexec_b64 s[6:7], vcc
	s_xor_b64 s[6:7], exec, s[6:7]
	s_cbranch_execz .LBB0_137
	s_waitcnt lgkmcnt(0)
	v_readlane_b32 s12, v243, 7
	v_readlane_b32 s13, v243, 8
	v_mad_u32_u24 v5, v2, v1, v1
	v_mov_b32_e32 v1, 0
	s_add_u32 s12, s12, 0x3400
	s_addc_u32 s13, s13, 0
	global_load_dword v1, v1, s[12:13] sc1
	s_waitcnt vmcnt(0)
	v_cmp_lt_u32_e32 vcc, v1, v5
	s_and_saveexec_b64 s[8:9], vcc
	s_cbranch_execz .LBB0_136
	s_load_dwordx4 s[16:19], s[96:97], 0xb8
	s_mov_b32 s24, 1
	s_mov_b64 s[14:15], 0
	v_mov_b32_e32 v1, 0
	s_waitcnt lgkmcnt(0)
	s_add_u32 s10, s16, 0x4200
	s_addc_u32 s11, s17, 0
	s_branch .LBB0_127

.LBB0_129:
	global_load_dword v3, v1, s[12:13] sc1
	s_add_i32 s24, s24, 1
	s_mov_b64 s[20:21], -1
	s_waitcnt vmcnt(0)
	v_cmp_ge_u32_e32 vcc, v3, v5
	s_orn2_b64 s[18:19], vcc, exec
	s_branch .LBB0_126

.LBB0_140:
	s_or_b64 exec, exec, s[8:9]
	v_cvt_f32_u32_e32 v4, v1
	s_waitcnt vmcnt(0)
	v_readfirstlane_b32 s6, v3
	s_load_dwordx4 s[8:11], s[96:97], 0xb8
	s_waitcnt lgkmcnt(0)
	s_mov_b64 s[10:11], -1
	v_rcp_iflag_f32_e32 v4, v4
	v_add_u32_e32 v2, s6, v2
	v_add_u32_e32 v5, 1, v2
	s_add_u32 s8, s8, 0x7400
	v_mul_f32_e32 v3, 0x4f7ffffe, v4
	v_cvt_u32_f32_e32 v3, v3
	v_sub_u32_e32 v4, 0, v1
	s_addc_u32 s9, s9, 0
	v_mul_lo_u32 v4, v4, v3
	v_mul_hi_u32 v4, v3, v4
	v_add_u32_e32 v3, v3, v4
	v_mul_hi_u32 v3, v2, v3
	v_mul_lo_u32 v4, v3, v1
	v_sub_u32_e32 v2, v2, v4
	v_add_u32_e32 v6, 1, v3
	v_cmp_ge_u32_e32 vcc, v2, v1
	v_sub_u32_e32 v4, v2, v1
	s_nop 0
	v_cndmask_b32_e32 v3, v3, v6, vcc
	v_cndmask_b32_e32 v2, v2, v4, vcc
	v_add_u32_e32 v4, 1, v3
	v_cmp_ge_u32_e32 vcc, v2, v1
	s_nop 1
	v_cndmask_b32_e32 v4, v3, v4, vcc
	v_mul_lo_u32 v2, v1, v4
	v_add_u32_e32 v1, v2, v1
	v_cmp_ne_u32_e32 vcc, v5, v1
	v_mov_b64_e32 v[2:3], s[8:9]
	s_and_saveexec_b64 s[6:7], vcc
	s_cbranch_execz .LBB0_152
	v_mov_b32_e32 v5, v1
	v_mov_b32_e32 v1, 0
	global_load_dword v2, v1, s[8:9] sc1
	s_mov_b64 s[14:15], 0
	s_waitcnt vmcnt(0)
	v_cmp_lt_u32_e32 vcc, v2, v5
	s_and_saveexec_b64 s[12:13], vcc
	s_cbranch_execz .LBB0_151
	s_load_dwordx4 s[16:19], s[96:97], 0xb8
	s_mov_b32 s24, 1
	s_waitcnt lgkmcnt(0)
	s_add_u32 s10, s16, 0x4200
	s_addc_u32 s11, s17, 0
	s_branch .LBB0_144

.LBB0_146:
	global_load_dword v2, v1, s[8:9] sc1
	s_add_i32 s24, s24, 1
	s_mov_b64 s[18:19], -1
	s_waitcnt vmcnt(0)
	v_cmp_ge_u32_e32 vcc, v2, v5
	s_orn2_b64 s[22:23], vcc, exec
	s_branch .LBB0_143

.LBB0_152:
	s_or_b64 exec, exec, s[6:7]
	s_and_saveexec_b64 s[6:7], s[10:11]
	s_cbranch_execz .LBB0_154
	v_mov_b32_e32 v1, 1
.LBB0_154:
	s_or_b64 exec, exec, s[6:7]
	s_mov_b64 s[6:7], exec
	v_mbcnt_lo_u32_b32 v1, s6, 0
	v_mbcnt_hi_u32_b32 v1, s7, v1
	v_cmp_eq_u32_e32 vcc, 0, v1
	s_waitcnt vmcnt(0)
	s_and_saveexec_b64 s[8:9], vcc
	s_cbranch_execz .LBB0_156
	s_bcnt1_i32_b64 s6, s[6:7]
	v_mov_b32_e32 v1, 0x2000
	v_mov_b32_e32 v2, s6
	global_atomic_add v1, v2, s[4:5] offset:1024

.LBB0_375:
	s_or_b64 exec, exec, s[6:7]
	s_and_saveexec_b64 s[6:7], s[10:11]
	s_cbranch_execz .LBB0_377
	v_mov_b32_e32 v1, 1
.LBB0_377:
	s_or_b64 exec, exec, s[6:7]
	s_mov_b64 s[6:7], exec
	v_mbcnt_lo_u32_b32 v1, s6, 0
	v_mbcnt_hi_u32_b32 v1, s7, v1
	v_cmp_eq_u32_e32 vcc, 0, v1
	s_waitcnt vmcnt(0)
	s_and_saveexec_b64 s[8:9], vcc
	s_cbranch_execz .LBB0_379
	s_bcnt1_i32_b64 s6, s[6:7]
	v_mov_b32_e32 v1, 0x2000
	v_mov_b32_e32 v2, s6
	global_atomic_add v1, v2, s[4:5] offset:1024

.LBB0_590:
	s_or_b64 exec, exec, s[6:7]
	s_and_saveexec_b64 s[6:7], s[10:11]
	s_cbranch_execz .LBB0_592
	v_mov_b32_e32 v1, 1
.LBB0_592:
	s_or_b64 exec, exec, s[6:7]
	s_mov_b64 s[6:7], exec
	v_mbcnt_lo_u32_b32 v1, s6, 0
	v_mbcnt_hi_u32_b32 v1, s7, v1
	v_cmp_eq_u32_e32 vcc, 0, v1
	s_waitcnt vmcnt(0)
	s_and_saveexec_b64 s[8:9], vcc
	s_cbranch_execz .LBB0_594
	s_bcnt1_i32_b64 s6, s[6:7]
	v_mov_b32_e32 v1, 0x2000
	v_mov_b32_e32 v2, s6
	global_atomic_add v1, v2, s[4:5] offset:1024

.LBB0_648:
	s_or_b64 exec, exec, s[6:7]
	s_and_saveexec_b64 s[6:7], s[10:11]
	s_cbranch_execz .LBB0_650
	v_mov_b32_e32 v1, 1
.LBB0_650:
	s_or_b64 exec, exec, s[6:7]
	s_mov_b64 s[6:7], exec
	v_mbcnt_lo_u32_b32 v1, s6, 0
	v_mbcnt_hi_u32_b32 v1, s7, v1
	v_cmp_eq_u32_e32 vcc, 0, v1
	s_waitcnt vmcnt(0)
	s_and_saveexec_b64 s[8:9], vcc
	s_cbranch_execz .LBB0_652
	s_bcnt1_i32_b64 s6, s[6:7]
	v_mov_b32_e32 v1, 0x2000
	v_mov_b32_e32 v2, s6
	global_atomic_add v1, v2, s[4:5] offset:1024

.LBB0_731:
	s_or_b64 exec, exec, s[6:7]
	s_and_saveexec_b64 s[6:7], s[10:11]
	s_cbranch_execz .LBB0_733
	v_mov_b32_e32 v1, 1
.LBB0_733:
	s_or_b64 exec, exec, s[6:7]
	s_mov_b64 s[6:7], exec
	v_mbcnt_lo_u32_b32 v1, s6, 0
	v_mbcnt_hi_u32_b32 v1, s7, v1
	v_cmp_eq_u32_e32 vcc, 0, v1
	s_waitcnt vmcnt(0)
	s_and_saveexec_b64 s[8:9], vcc
	s_cbranch_execz .LBB0_735
	s_bcnt1_i32_b64 s6, s[6:7]
	v_mov_b32_e32 v1, 0x2000
	v_mov_b32_e32 v2, s6
	global_atomic_add v1, v2, s[4:5] offset:1024

.LBB0_812:
	s_or_b64 exec, exec, s[6:7]
	s_and_saveexec_b64 s[6:7], s[10:11]
	s_cbranch_execz .LBB0_814
	v_mov_b32_e32 v1, 1
.LBB0_814:
	s_or_b64 exec, exec, s[6:7]
	s_mov_b64 s[6:7], exec
	v_mbcnt_lo_u32_b32 v1, s6, 0
	v_mbcnt_hi_u32_b32 v1, s7, v1
	v_cmp_eq_u32_e32 vcc, 0, v1
	s_waitcnt vmcnt(0)
	s_and_saveexec_b64 s[8:9], vcc
	s_cbranch_execz .LBB0_816
	s_bcnt1_i32_b64 s6, s[6:7]
	v_mov_b32_e32 v1, 0x2000
	v_mov_b32_e32 v2, s6
	global_atomic_add v1, v2, s[4:5] offset:1024

.LBB0_864:
	s_or_b64 exec, exec, s[8:9]
	v_cvt_f32_u32_e32 v5, v3
	s_waitcnt vmcnt(0)
	v_readfirstlane_b32 s6, v4
	v_sub_u32_e32 v4, 0, v3
	v_rcp_iflag_f32_e32 v5, v5
	v_add_u32_e32 v6, s6, v2
	v_mul_f32_e32 v5, 0x4f7ffffe, v5
	v_cvt_u32_f32_e32 v5, v5
	v_mul_lo_u32 v2, v4, v5
	v_mul_hi_u32 v2, v5, v2
	v_add_u32_e32 v2, v5, v2
	v_mul_hi_u32 v2, v6, v2
	v_mul_lo_u32 v4, v2, v3
	v_sub_u32_e32 v4, v6, v4
	v_add_u32_e32 v5, 1, v2
	v_cmp_ge_u32_e32 vcc, v4, v3
	s_nop 1
	v_cndmask_b32_e32 v2, v2, v5, vcc
	v_sub_u32_e32 v5, v4, v3
	v_cndmask_b32_e32 v4, v4, v5, vcc
	v_add_u32_e32 v5, 1, v2
	v_cmp_ge_u32_e32 vcc, v4, v3
	v_add_u32_e32 v4, 1, v6
	s_nop 0
	v_cndmask_b32_e32 v2, v2, v5, vcc
	v_mul_lo_u32 v5, v3, v2
	v_add_u32_e32 v3, v5, v3
	v_cmp_ne_u32_e32 vcc, v4, v3
	s_and_saveexec_b64 s[6:7], vcc
	s_xor_b64 s[6:7], exec, s[6:7]
	s_cbranch_execz .LBB0_878
	s_waitcnt lgkmcnt(0)
	v_readlane_b32 s12, v243, 7
	v_readlane_b32 s13, v243, 8
	v_mad_u32_u24 v5, v2, v1, v1
	v_mov_b32_e32 v1, 0
	s_add_u32 s12, s12, 0x3400
	s_addc_u32 s13, s13, 0
	global_load_dword v1, v1, s[12:13] sc1
	s_waitcnt vmcnt(0)
	v_cmp_lt_u32_e32 vcc, v1, v5
	s_and_saveexec_b64 s[8:9], vcc
	s_cbranch_execz .LBB0_877
	v_readlane_b32 s16, v243, 0
	v_readlane_b32 s17, v243, 1
	s_add_u32 s10, s16, 0x4200
	s_addc_u32 s11, s17, 0
	s_mov_b32 s24, 1
	s_mov_b64 s[14:15], 0
	v_mov_b32_e32 v1, 0
	v_readlane_b32 s18, v243, 2
	v_readlane_b32 s19, v243, 3
	s_branch .LBB0_868

.LBB0_881:
	s_or_b64 exec, exec, s[8:9]
	v_cvt_f32_u32_e32 v4, v1
	s_waitcnt vmcnt(0)
	v_readfirstlane_b32 s6, v3
	v_readlane_b32 s8, v243, 0
	v_readlane_b32 s9, v243, 1
	v_rcp_iflag_f32_e32 v4, v4
	v_add_u32_e32 v2, s6, v2
	v_add_u32_e32 v5, 1, v2
	s_add_u32 s8, s8, 0x7400
	v_mul_f32_e32 v3, 0x4f7ffffe, v4
	v_cvt_u32_f32_e32 v3, v3
	v_sub_u32_e32 v4, 0, v1
	v_readlane_b32 s10, v243, 2
	v_readlane_b32 s11, v243, 3
	v_mul_lo_u32 v4, v4, v3
	v_mul_hi_u32 v4, v3, v4
	v_add_u32_e32 v3, v3, v4
	v_mul_hi_u32 v3, v2, v3
	v_mul_lo_u32 v4, v3, v1
	v_sub_u32_e32 v2, v2, v4
	v_add_u32_e32 v6, 1, v3
	v_cmp_ge_u32_e32 vcc, v2, v1
	v_sub_u32_e32 v4, v2, v1
	s_addc_u32 s9, s9, 0
	v_cndmask_b32_e32 v3, v3, v6, vcc
	v_cndmask_b32_e32 v2, v2, v4, vcc
	v_add_u32_e32 v4, 1, v3
	v_cmp_ge_u32_e32 vcc, v2, v1
	s_mov_b64 s[10:11], -1
	s_nop 0
	v_cndmask_b32_e32 v4, v3, v4, vcc
	v_mul_lo_u32 v2, v1, v4
	v_add_u32_e32 v1, v2, v1
	v_cmp_ne_u32_e32 vcc, v5, v1
	v_mov_b64_e32 v[2:3], s[8:9]
	s_and_saveexec_b64 s[6:7], vcc
	s_cbranch_execz .LBB0_893
	v_mov_b32_e32 v5, v1
	v_mov_b32_e32 v1, 0
	global_load_dword v2, v1, s[8:9] sc1
	s_mov_b64 s[14:15], 0
	s_waitcnt vmcnt(0)
	v_cmp_lt_u32_e32 vcc, v2, v5
	s_and_saveexec_b64 s[12:13], vcc
	s_cbranch_execz .LBB0_892
	v_readlane_b32 s16, v243, 0
	v_readlane_b32 s17, v243, 1
	s_add_u32 s10, s16, 0x4200
	s_addc_u32 s11, s17, 0
	s_mov_b32 s24, 1
	v_readlane_b32 s18, v243, 2
	v_readlane_b32 s19, v243, 3
	s_branch .LBB0_885

.LBB0_893:
	s_or_b64 exec, exec, s[6:7]
	s_and_saveexec_b64 s[6:7], s[10:11]
	s_cbranch_execz .LBB0_895
	v_mov_b32_e32 v1, 1
.LBB0_895:
	s_or_b64 exec, exec, s[6:7]
	s_mov_b64 s[6:7], exec
	v_mbcnt_lo_u32_b32 v1, s6, 0
	v_mbcnt_hi_u32_b32 v1, s7, v1
	v_cmp_eq_u32_e32 vcc, 0, v1
	s_waitcnt vmcnt(0)
	s_and_saveexec_b64 s[8:9], vcc
	s_cbranch_execz .LBB0_897
	s_bcnt1_i32_b64 s6, s[6:7]
	v_mov_b32_e32 v1, 0x2000
	v_mov_b32_e32 v2, s6
	global_atomic_add v1, v2, s[4:5] offset:1024

.LBB0_978:
	s_or_b64 exec, exec, s[6:7]
	s_and_saveexec_b64 s[6:7], s[10:11]
	s_cbranch_execz .LBB0_980
	v_mov_b32_e32 v1, 1
.LBB0_980:
	s_or_b64 exec, exec, s[6:7]
	s_mov_b64 s[6:7], exec
	v_mbcnt_lo_u32_b32 v1, s6, 0
	v_mbcnt_hi_u32_b32 v1, s7, v1
	v_cmp_eq_u32_e32 vcc, 0, v1
	s_waitcnt vmcnt(0)
	s_and_saveexec_b64 s[8:9], vcc
	s_cbranch_execz .LBB0_982
	s_bcnt1_i32_b64 s6, s[6:7]
	v_mov_b32_e32 v1, 0x2000
	v_mov_b32_e32 v2, s6
	global_atomic_add v1, v2, s[4:5] offset:1024

.LBB0_1128:
	s_or_b64 exec, exec, s[6:7]
	s_and_saveexec_b64 s[6:7], s[10:11]
	s_cbranch_execz .LBB0_1130
	v_mov_b32_e32 v1, 1
.LBB0_1130:
	s_or_b64 exec, exec, s[6:7]
	s_mov_b64 s[6:7], exec
	v_mbcnt_lo_u32_b32 v1, s6, 0
	v_mbcnt_hi_u32_b32 v1, s7, v1
	v_cmp_eq_u32_e32 vcc, 0, v1
	s_waitcnt vmcnt(0)
	s_and_saveexec_b64 s[8:9], vcc
	s_cbranch_execz .LBB0_1132
	s_bcnt1_i32_b64 s6, s[6:7]
	v_mov_b32_e32 v1, 0x2000
	v_mov_b32_e32 v2, s6
	global_atomic_add v1, v2, s[4:5] offset:1024

.LBB0_1197:
	s_or_b64 exec, exec, s[6:7]
	s_and_saveexec_b64 s[6:7], s[10:11]
	s_cbranch_execz .LBB0_1199
	v_mov_b32_e32 v1, 1
.LBB0_1199:
	s_or_b64 exec, exec, s[6:7]
	s_mov_b64 s[6:7], exec
	v_mbcnt_lo_u32_b32 v1, s6, 0
	v_mbcnt_hi_u32_b32 v1, s7, v1
	v_cmp_eq_u32_e32 vcc, 0, v1
	s_waitcnt vmcnt(0)
	s_and_saveexec_b64 s[8:9], vcc
	s_cbranch_execz .LBB0_1201
	s_bcnt1_i32_b64 s6, s[6:7]
	v_mov_b32_e32 v1, 0x2000
	v_mov_b32_e32 v2, s6
	global_atomic_add v1, v2, s[4:5] offset:1024
